# speedup vs baseline: 1.0044x; 1.0044x over previous
.LBB6_55:
	s_and_b64 vcc, exec, s[16:17]
	s_cbranch_vccz .LBB6_9
	s_waitcnt vmcnt(7)
	v_cvt_f32_f16_e32 v6, v24
	s_waitcnt vmcnt(6)
	v_cvt_f32_f16_e32 v7, v23
	v_cmp_gt_i32_e32 vcc, s58, v81
	s_waitcnt vmcnt(5)
	s_and_saveexec_b64 s[16:17], s[0:1]
	ds_write_b32 v92, v21
	ds_write_b32 v92, v20 offset:64
	s_or_b64 exec, exec, s[16:17]
	s_add_i32 s22, s58, 3
	s_ashr_i32 s22, s22, 2
	s_min_u32 s17, s22, 4
	s_lshl_b32 s22, s17, 4
	s_add_i32 s22, s22, -64
	v_add_u32_e32 v38, s22, v94
	ds_read2_b32 v[30:31], v38 offset0:0 offset1:2
	ds_read2_b32 v[32:33], v38 offset0:4 offset1:6
	ds_read2_b32 v[34:35], v38 offset0:8 offset1:10
	ds_read2_b32 v[36:37], v38 offset0:12 offset1:14
	s_waitcnt lgkmcnt(0)
	s_cmp_eq_u32 s17, 1
	s_cbranch_scc1 .Le1_i0
	s_cmp_eq_u32 s17, 2
	s_cbranch_scc1 .Le1_i1
	s_cmp_eq_u32 s17, 3
	s_cbranch_scc1 .Le1_i2
	v_lshl_or_b32 v30, v30, 9, v88
	v_lshl_or_b32 v31, v31, 9, v88
	buffer_load_dwordx4 v[66:69], v30, s[24:27], 0 offen sc0 sc1
	buffer_load_dwordx4 v[62:65], v31, s[24:27], 0 offen sc0 sc1
.Le1_i2:
	v_lshl_or_b32 v32, v32, 9, v88
	v_lshl_or_b32 v33, v33, 9, v88
	buffer_load_dwordx4 v[58:61], v32, s[24:27], 0 offen sc0 sc1
	buffer_load_dwordx4 v[54:57], v33, s[24:27], 0 offen sc0 sc1
.Le1_i1:
	v_lshl_or_b32 v34, v34, 9, v88
	v_lshl_or_b32 v35, v35, 9, v88
	buffer_load_dwordx4 v[50:53], v34, s[24:27], 0 offen sc0 sc1
	buffer_load_dwordx4 v[46:49], v35, s[24:27], 0 offen sc0 sc1
.Le1_i0:
	v_lshl_or_b32 v36, v36, 9, v88
	v_lshl_or_b32 v37, v37, 9, v88
	buffer_load_dwordx4 v[42:45], v36, s[24:27], 0 offen sc0 sc1
	buffer_load_dwordx4 v[38:41], v37, s[24:27], 0 offen sc0 sc1
	v_add_f32_e32 v6, v22, v6
	v_add_f32_e32 v7, v22, v7
	v_mul_f32_e32 v8, 0x3e4ccccd, v6
	v_max_f32_e32 v6, v6, v8
	v_mul_f32_e32 v8, 0x3e4ccccd, v7
	v_cndmask_b32_e32 v6, v14, v6, vcc
	v_max_f32_e32 v7, v7, v8
	v_cmp_gt_i32_e32 vcc, s58, v82
	s_nop 1
	v_cndmask_b32_e32 v7, v14, v7, vcc
	v_max_f32_e32 v8, v6, v7
	s_nop 1
	v_max_f32_dpp v8, v8, v8 quad_perm:[1,0,3,2] row_mask:0xf bank_mask:0xf
	s_nop 0
	s_nop 1
	v_max_f32_dpp v8, v8, v8 quad_perm:[2,3,0,1] row_mask:0xf bank_mask:0xf
	s_nop 0
	s_nop 1
	v_max_f32_dpp v8, v8, v8 row_half_mirror row_mask:0xf bank_mask:0xf
	s_nop 0
	s_nop 1
	v_max_f32_dpp v8, v8, v8 row_mirror row_mask:0xf bank_mask:0xf
	s_nop 0
	v_sub_f32_e32 v6, v6, v8
	v_mul_f32_e32 v6, 0x3fb8aa3b, v6
	v_exp_f32_e32 v9, v6
	v_sub_f32_e32 v6, v7, v8
	v_mul_f32_e32 v6, 0x3fb8aa3b, v6
	v_exp_f32_e32 v6, v6
	s_nop 0
	v_add_f32_e32 v7, v9, v6
	s_nop 1
	v_add_f32_dpp v7, v7, v7 quad_perm:[1,0,3,2] row_mask:0xf bank_mask:0xf
	s_nop 0
	s_nop 1
	v_add_f32_dpp v7, v7, v7 quad_perm:[2,3,0,1] row_mask:0xf bank_mask:0xf
	s_nop 0
	s_nop 1
	v_add_f32_dpp v7, v7, v7 row_half_mirror row_mask:0xf bank_mask:0xf
	s_nop 0
	s_nop 1
	v_add_f32_dpp v7, v7, v7 row_mirror row_mask:0xf bank_mask:0xf
	s_nop 0
	v_rcp_f32_e32 v7, v7
	s_nop 0
	v_mul_f32_e32 v8, v9, v7
	ds_write_b32 v91, v8
	s_cmp_lt_i32 s58, 17
	s_cbranch_scc1 .LBB6_62
	v_mul_f32_e32 v6, v6, v7
	ds_write_b32 v93, v6
.LBB6_62:
	s_add_i32 s58, s58, 3
	s_ashr_i32 s58, s58, 2
	s_cmp_lt_i32 s58, 1
	s_cbranch_scc1 .LBB6_8
	v_mov_b32_e32 v70, 0
	v_mov_b32_e32 v71, 0
	v_mov_b32_e32 v72, 0
	v_mov_b32_e32 v73, 0
	v_mov_b32_e32 v74, 0
	v_mov_b32_e32 v75, 0
	v_mov_b32_e32 v76, 0
	v_mov_b32_e32 v77, 0
	s_min_u32 s17, s58, 4
	s_lshl_b32 s22, s17, 4
	s_add_i32 s22, s22, -64
	s_lshl_b32 s22, s22, 2
	v_add_u32_e32 v6, s22, v95
	ds_read2_b32 v[30:31], v6 offset0:0 offset1:8
	ds_read2_b32 v[32:33], v6 offset0:16 offset1:24
	ds_read2_b32 v[34:35], v6 offset0:32 offset1:40
	ds_read2_b32 v[36:37], v6 offset0:48 offset1:56
	s_waitcnt lgkmcnt(0)
	s_cmp_eq_u32 s17, 1
	s_cbranch_scc1 .Lagg1f_b0_f0
	s_cmp_eq_u32 s17, 2
	s_cbranch_scc1 .Lagg1f_b0_f1
	s_cmp_eq_u32 s17, 3
	s_cbranch_scc1 .Lagg1f_b0_f2
	s_waitcnt vmcnt(7)
	v_fma_mix_f32 v70, v30, v66, v70 op_sel_hi:[0,1,0]
	v_fma_mix_f32 v71, v30, v66, v71 op_sel:[0,1,0] op_sel_hi:[0,1,0]
	v_fma_mix_f32 v72, v30, v67, v72 op_sel_hi:[0,1,0]
	v_fma_mix_f32 v73, v30, v67, v73 op_sel:[0,1,0] op_sel_hi:[0,1,0]
	v_fma_mix_f32 v74, v30, v68, v74 op_sel_hi:[0,1,0]
	v_fma_mix_f32 v75, v30, v68, v75 op_sel:[0,1,0] op_sel_hi:[0,1,0]
	v_fma_mix_f32 v76, v30, v69, v76 op_sel_hi:[0,1,0]
	v_fma_mix_f32 v77, v30, v69, v77 op_sel:[0,1,0] op_sel_hi:[0,1,0]
	s_waitcnt vmcnt(6)
	v_fma_mix_f32 v70, v31, v62, v70 op_sel_hi:[0,1,0]
	v_fma_mix_f32 v71, v31, v62, v71 op_sel:[0,1,0] op_sel_hi:[0,1,0]
	v_fma_mix_f32 v72, v31, v63, v72 op_sel_hi:[0,1,0]
	v_fma_mix_f32 v73, v31, v63, v73 op_sel:[0,1,0] op_sel_hi:[0,1,0]
	v_fma_mix_f32 v74, v31, v64, v74 op_sel_hi:[0,1,0]
	v_fma_mix_f32 v75, v31, v64, v75 op_sel:[0,1,0] op_sel_hi:[0,1,0]
	v_fma_mix_f32 v76, v31, v65, v76 op_sel_hi:[0,1,0]
	v_fma_mix_f32 v77, v31, v65, v77 op_sel:[0,1,0] op_sel_hi:[0,1,0]
